# grid barrier: generation from a per-workgroup LDS counter instead of dividing the arrival count (shorter path to the leader's write-back + arrival)
# baseline (speedup 1.0000x reference)
.LBB0_600:
	s_cmp_eq_u32 s2, 3
	s_cselect_b64 s[0:1], -1, 0
	v_writelane_b32 v253, s0, 63
	s_nop 1
	v_writelane_b32 v254, s1, 0
	s_and_b64 s[0:1], s[0:1], exec
	s_cselect_b32 s3, 0, s2
	s_lshl_b32 s0, s2, 3
	s_or_b32 s60, s0, 1
	v_writelane_b32 v254, s2, 1
	s_cmp_eq_u32 s3, 0
	v_writelane_b32 v254, s0, 2
	s_cselect_b64 s[0:1], -1, 0
	v_writelane_b32 v254, s0, 3
	s_cmp_lg_u32 s3, 0
	s_nop 0
	v_writelane_b32 v254, s1, 4
	v_writelane_b32 v254, s3, 5
	s_cbranch_scc1 .LBB0_1779
	v_readlane_b32 s6, v253, 3
	v_readlane_b32 s7, v253, 4
	s_cmp_lt_i32 s60, s6
	s_cselect_b64 s[0:1], -1, 0
	s_cmp_ge_i32 s60, s7
	s_cselect_b64 s[2:3], -1, 0
	s_or_b64 s[0:1], s[0:1], s[2:3]
	s_and_b64 vcc, exec, s[0:1]
	s_cbranch_vccnz .LBB0_968
	v_readlane_b32 s0, v254, 2
	s_cmp_lt_i32 s0, s6
	v_readlane_b32 s22, v254, 1
	s_cbranch_scc1 .LBB0_651
	s_waitcnt vmcnt(0)
	s_barrier
	s_mov_b64 s[0:1], exec
	v_readlane_b32 s2, v253, 1
	v_readlane_b32 s3, v253, 2
	s_and_b64 s[2:3], s[0:1], s[2:3]
	s_mov_b64 exec, s[2:3]
	s_cbranch_execz .LBB0_650
	v_readlane_b32 s4, v253, 36
	v_readlane_b32 s6, v253, 11
	v_readlane_b32 s7, v253, 12
	v_readlane_b32 s8, v253, 7
	v_readlane_b32 s9, v253, 8
	s_waitcnt vmcnt(0) lgkmcnt(0)
	v_mov_b32_e32 v1, s4
	ds_read2_b32 v[2:3], v1 offset1:1
	ds_read_b32 v7, v1 offset:8
	global_atomic_add v4, v87, v230, s[8:9] sc0
	s_waitcnt lgkmcnt(0)
	v_add_u32_e32 v7, 1, v7
	ds_write_b32 v1, v7 offset:8
	v_max_u32_e32 v2, 1, v2
	v_max_u32_e32 v3, 1, v3
	v_add_u32_e32 v6, 1, v7
	v_mul_lo_u32 v5, v6, v3
	v_mul_lo_u32 v6, v6, v2
	s_waitcnt vmcnt(0)
	v_add_u32_e32 v4, 1, v4
	v_cmp_ne_u32_e32 vcc, v4, v6
	s_cbranch_vccnz .Lxb_poll_0
	buffer_wbl2 sc1
	s_waitcnt vmcnt(0)
	global_atomic_add v87, v230, s[6:7]
.Lxb_poll_0:
	s_mov_b32 s11, 0
	global_load_dword v2, v87, s[6:7] sc1
	s_sleep 24
.Lxb_spin_0:
	global_load_dword v4, v87, s[6:7] sc1
	s_waitcnt vmcnt(1)
	v_cmp_le_u32_e32 vcc, v5, v2
	s_cbranch_vccnz .Lxb_done_0
	global_load_dword v2, v87, s[6:7] sc1
	s_waitcnt vmcnt(1)
	v_cmp_le_u32_e32 vcc, v5, v4
	s_cbranch_vccnz .Lxb_done_0
	s_add_i32 s11, s11, 1
	s_cmp_lt_u32 s11, 0x40000
	s_cbranch_scc1 .Lxb_spin_0

.LBB0_968:
	v_readlane_b32 s0, v254, 2
	s_or_b32 s0, s0, 2
	s_cmp_lt_i32 s0, s6
	s_cselect_b64 s[2:3], -1, 0
	s_cmp_ge_i32 s0, s7
	s_cselect_b64 s[4:5], -1, 0
	s_or_b64 s[2:3], s[2:3], s[4:5]
	s_and_b64 vcc, exec, s[2:3]
	s_cbranch_vccnz .LBB0_1432
	s_cmp_le_i32 s0, s6
	s_cbranch_scc1 .LBB0_1008
	s_waitcnt vmcnt(0)
	s_waitcnt vmcnt(0) lgkmcnt(0)
	s_barrier
	s_mov_b64 s[0:1], exec
	v_readlane_b32 s2, v253, 1
	v_readlane_b32 s3, v253, 2
	s_and_b64 s[2:3], s[0:1], s[2:3]
	s_mov_b64 exec, s[2:3]
	s_cbranch_execz .LBB0_1007
	v_readlane_b32 s4, v253, 36
	v_readlane_b32 s6, v253, 11
	v_readlane_b32 s7, v253, 12
	v_readlane_b32 s8, v253, 7
	v_readlane_b32 s9, v253, 8
	s_waitcnt vmcnt(0) lgkmcnt(0)
	v_mov_b32_e32 v1, s4
	ds_read2_b32 v[2:3], v1 offset1:1
	ds_read_b32 v7, v1 offset:8
	global_atomic_add v4, v87, v230, s[8:9] sc0
	s_waitcnt lgkmcnt(0)
	v_add_u32_e32 v7, 1, v7
	ds_write_b32 v1, v7 offset:8
	v_max_u32_e32 v2, 1, v2
	v_max_u32_e32 v3, 1, v3
	v_add_u32_e32 v6, 1, v7
	v_mul_lo_u32 v5, v6, v3
	v_mul_lo_u32 v6, v6, v2
	s_waitcnt vmcnt(0)
	v_add_u32_e32 v4, 1, v4
	v_cmp_ne_u32_e32 vcc, v4, v6
	s_cbranch_vccnz .Lxb_poll_1
	buffer_wbl2 sc1
	s_waitcnt vmcnt(0)
	global_atomic_add v87, v230, s[6:7]

.LBB0_1432:
	v_readlane_b32 s0, v254, 2
	s_or_b32 s0, s0, 3
	s_cmp_lt_i32 s0, s6
	s_cselect_b64 s[2:3], -1, 0
	s_cmp_ge_i32 s0, s7
	s_cselect_b64 s[4:5], -1, 0
	s_or_b64 s[2:3], s[2:3], s[4:5]
	s_and_b64 vcc, exec, s[2:3]
	s_cbranch_vccnz .LBB0_1779
	v_readlane_b32 s2, v253, 3
	s_cmp_le_i32 s0, s2
	v_readlane_b32 s3, v253, 4
	s_cbranch_scc1 .LBB0_1472
	s_waitcnt vmcnt(0)
	s_waitcnt vmcnt(0) lgkmcnt(0)
	s_barrier
	s_mov_b64 s[0:1], exec
	v_readlane_b32 s2, v253, 1
	v_readlane_b32 s3, v253, 2
	s_and_b64 s[2:3], s[0:1], s[2:3]
	s_mov_b64 exec, s[2:3]
	s_cbranch_execz .LBB0_1471
	v_readlane_b32 s4, v253, 36
	v_readlane_b32 s6, v253, 11
	v_readlane_b32 s7, v253, 12
	v_readlane_b32 s8, v253, 7
	v_readlane_b32 s9, v253, 8
	s_waitcnt vmcnt(0) lgkmcnt(0)
	v_mov_b32_e32 v1, s4
	ds_read2_b32 v[2:3], v1 offset1:1
	ds_read_b32 v7, v1 offset:8
	global_atomic_add v4, v87, v230, s[8:9] sc0
	s_waitcnt lgkmcnt(0)
	v_add_u32_e32 v7, 1, v7
	ds_write_b32 v1, v7 offset:8
	v_max_u32_e32 v2, 1, v2
	v_max_u32_e32 v3, 1, v3
	v_add_u32_e32 v6, 1, v7
	v_mul_lo_u32 v5, v6, v3
	v_mul_lo_u32 v6, v6, v2
	s_waitcnt vmcnt(0)
	v_add_u32_e32 v4, 1, v4
	v_cmp_ne_u32_e32 vcc, v4, v6
	s_cbranch_vccnz .Lxb_poll_2
	buffer_wbl2 sc1
	s_waitcnt vmcnt(0)
	global_atomic_add v87, v230, s[6:7]

.LBB0_1779:
	v_readlane_b32 s0, v254, 5
	s_cmp_eq_u32 s0, 1
	s_cselect_b64 s[2:3], -1, 0
	v_writelane_b32 v254, s2, 6
	s_cmp_lg_u32 s0, 1
	s_nop 0
	v_writelane_b32 v254, s3, 7
	s_cbranch_scc1 .LBB0_2204
	v_readlane_b32 s4, v253, 3
	v_readlane_b32 s5, v253, 4
	s_cmp_lt_i32 s60, s4
	s_cselect_b64 s[0:1], -1, 0
	s_cmp_ge_i32 s60, s5
	s_cselect_b64 s[2:3], -1, 0
	s_or_b64 s[0:1], s[0:1], s[2:3]
	s_and_b64 vcc, exec, s[0:1]
	s_cbranch_vccnz .LBB0_1832
	v_readlane_b32 s0, v254, 2
	s_cmp_lt_i32 s0, s4
	s_cbranch_scc1 .LBB0_1820
	s_waitcnt vmcnt(0)
	s_waitcnt vmcnt(0) lgkmcnt(0)
	s_barrier
	s_mov_b64 s[0:1], exec
	v_readlane_b32 s2, v253, 1
	v_readlane_b32 s3, v253, 2
	v_readlane_b32 s18, v253, 61
	s_and_b64 s[2:3], s[0:1], s[2:3]
	v_readlane_b32 s19, v253, 62
	s_mov_b64 exec, s[2:3]
	s_cbranch_execz .LBB0_1819
	v_readlane_b32 s4, v253, 36
	v_readlane_b32 s6, v253, 11
	v_readlane_b32 s7, v253, 12
	v_readlane_b32 s8, v253, 7
	v_readlane_b32 s9, v253, 8
	s_waitcnt vmcnt(0) lgkmcnt(0)
	v_mov_b32_e32 v1, s4
	ds_read2_b32 v[2:3], v1 offset1:1
	ds_read_b32 v7, v1 offset:8
	global_atomic_add v4, v87, v230, s[8:9] sc0
	s_waitcnt lgkmcnt(0)
	v_add_u32_e32 v7, 1, v7
	ds_write_b32 v1, v7 offset:8
	v_max_u32_e32 v2, 1, v2
	v_max_u32_e32 v3, 1, v3
	v_add_u32_e32 v6, 1, v7
	v_mul_lo_u32 v5, v6, v3
	v_mul_lo_u32 v6, v6, v2
	s_waitcnt vmcnt(0)
	v_add_u32_e32 v4, 1, v4
	v_cmp_ne_u32_e32 vcc, v4, v6
	s_cbranch_vccnz .Lxb_poll_3
	buffer_wbl2 sc1
	s_waitcnt vmcnt(0)
	global_atomic_add v87, v230, s[6:7]

.LBB0_1832:
	v_readlane_b32 s0, v254, 2
	s_or_b32 s0, s0, 3
	s_cmp_lt_i32 s0, s4
	s_cselect_b64 s[2:3], -1, 0
	s_cmp_ge_i32 s0, s5
	s_cselect_b64 s[4:5], -1, 0
	s_or_b64 s[2:3], s[2:3], s[4:5]
	s_and_b64 vcc, exec, s[2:3]
	s_cbranch_vccnz .LBB0_2204
	v_readlane_b32 s2, v253, 3
	s_cmp_le_i32 s0, s2
	v_readlane_b32 s3, v253, 4
	s_cbranch_scc1 .LBB0_1872
	s_waitcnt vmcnt(0)
	s_waitcnt vmcnt(0) lgkmcnt(0)
	s_barrier
	s_mov_b64 s[0:1], exec
	v_readlane_b32 s2, v253, 1
	v_readlane_b32 s3, v253, 2
	v_readlane_b32 s18, v253, 61
	s_and_b64 s[2:3], s[0:1], s[2:3]
	v_readlane_b32 s19, v253, 62
	s_mov_b64 exec, s[2:3]
	s_cbranch_execz .LBB0_1871
	v_readlane_b32 s4, v253, 36
	v_readlane_b32 s6, v253, 11
	v_readlane_b32 s7, v253, 12
	v_readlane_b32 s8, v253, 7
	v_readlane_b32 s9, v253, 8
	s_waitcnt vmcnt(0) lgkmcnt(0)
	v_mov_b32_e32 v1, s4
	ds_read2_b32 v[2:3], v1 offset1:1
	ds_read_b32 v7, v1 offset:8
	global_atomic_add v4, v87, v230, s[8:9] sc0
	s_waitcnt lgkmcnt(0)
	v_add_u32_e32 v7, 1, v7
	ds_write_b32 v1, v7 offset:8
	v_max_u32_e32 v2, 1, v2
	v_max_u32_e32 v3, 1, v3
	v_add_u32_e32 v6, 1, v7
	v_mul_lo_u32 v5, v6, v3
	v_mul_lo_u32 v6, v6, v2
	s_waitcnt vmcnt(0)
	v_add_u32_e32 v4, 1, v4
	v_cmp_ne_u32_e32 vcc, v4, v6
	s_cbranch_vccnz .Lxb_poll_4
	buffer_wbl2 sc1
	s_waitcnt vmcnt(0)
	global_atomic_add v87, v230, s[6:7]

.LBB0_2204:
	v_readlane_b32 s0, v254, 5
	s_cmp_lg_u32 s0, 2
	s_cbranch_scc1 .LBB0_3126
	v_readlane_b32 s6, v253, 3
	v_readlane_b32 s7, v253, 4
	s_cmp_lt_i32 s60, s6
	s_cselect_b64 s[0:1], -1, 0
	s_cmp_ge_i32 s60, s7
	s_cselect_b64 s[2:3], -1, 0
	s_or_b64 s[0:1], s[0:1], s[2:3]
	s_and_b64 vcc, exec, s[0:1]
	s_cbranch_vccnz .LBB0_2673
	v_readlane_b32 s0, v254, 2
	v_readlane_b32 s18, v253, 61
	s_cmp_lt_i32 s0, s6
	v_readlane_b32 s19, v253, 62
	s_cbranch_scc1 .LBB0_2245
	s_waitcnt vmcnt(0)
	s_waitcnt vmcnt(0) lgkmcnt(0)
	s_barrier
	s_mov_b64 s[0:1], exec
	v_readlane_b32 s2, v253, 1
	v_readlane_b32 s3, v253, 2
	s_and_b64 s[2:3], s[0:1], s[2:3]
	s_mov_b64 exec, s[2:3]
	s_cbranch_execz .LBB0_2244
	v_readlane_b32 s4, v253, 36
	v_readlane_b32 s6, v253, 11
	v_readlane_b32 s7, v253, 12
	v_readlane_b32 s8, v253, 7
	v_readlane_b32 s9, v253, 8
	s_waitcnt vmcnt(0) lgkmcnt(0)
	v_mov_b32_e32 v1, s4
	ds_read2_b32 v[2:3], v1 offset1:1
	ds_read_b32 v7, v1 offset:8
	global_atomic_add v4, v87, v230, s[8:9] sc0
	s_waitcnt lgkmcnt(0)
	v_add_u32_e32 v7, 1, v7
	ds_write_b32 v1, v7 offset:8
	v_max_u32_e32 v2, 1, v2
	v_max_u32_e32 v3, 1, v3
	v_add_u32_e32 v6, 1, v7
	v_mul_lo_u32 v5, v6, v3
	v_mul_lo_u32 v6, v6, v2
	s_waitcnt vmcnt(0)
	v_add_u32_e32 v4, 1, v4
	v_cmp_ne_u32_e32 vcc, v4, v6
	s_cbranch_vccnz .Lxb_poll_5
	buffer_wbl2 sc1
	s_waitcnt vmcnt(0)
	global_atomic_add v87, v230, s[6:7]

.LBB0_2673:
	v_readlane_b32 s0, v254, 2
	s_or_b32 s0, s0, 2
	s_cmp_lt_i32 s0, s6
	s_cselect_b64 s[2:3], -1, 0
	s_cmp_ge_i32 s0, s7
	s_cselect_b64 s[4:5], -1, 0
	s_or_b64 s[2:3], s[2:3], s[4:5]
	s_and_b64 vcc, exec, s[2:3]
	s_cbranch_vccnz .LBB0_3029
	v_readlane_b32 s18, v253, 61
	s_cmp_le_i32 s0, s6
	v_readlane_b32 s19, v253, 62
	s_cbranch_scc1 .LBB0_2713
	s_waitcnt vmcnt(0)
	s_waitcnt vmcnt(0) lgkmcnt(0)
	s_barrier
	s_mov_b64 s[0:1], exec
	v_readlane_b32 s2, v253, 1
	v_readlane_b32 s3, v253, 2
	s_and_b64 s[2:3], s[0:1], s[2:3]
	s_mov_b64 exec, s[2:3]
	s_cbranch_execz .LBB0_2712
	v_readlane_b32 s4, v253, 36
	v_readlane_b32 s6, v253, 11
	v_readlane_b32 s7, v253, 12
	v_readlane_b32 s8, v253, 7
	v_readlane_b32 s9, v253, 8
	s_waitcnt vmcnt(0) lgkmcnt(0)
	v_mov_b32_e32 v1, s4
	ds_read2_b32 v[2:3], v1 offset1:1
	ds_read_b32 v7, v1 offset:8
	global_atomic_add v4, v87, v230, s[8:9] sc0
	s_waitcnt lgkmcnt(0)
	v_add_u32_e32 v7, 1, v7
	ds_write_b32 v1, v7 offset:8
	v_max_u32_e32 v2, 1, v2
	v_max_u32_e32 v3, 1, v3
	v_add_u32_e32 v6, 1, v7
	v_mul_lo_u32 v5, v6, v3
	v_mul_lo_u32 v6, v6, v2
	s_waitcnt vmcnt(0)
	v_add_u32_e32 v4, 1, v4
	v_cmp_ne_u32_e32 vcc, v4, v6
	s_cbranch_vccnz .Lxb_poll_6
	buffer_wbl2 sc1
	s_waitcnt vmcnt(0)
	global_atomic_add v87, v230, s[6:7]

.LBB0_3029:
	v_readlane_b32 s0, v254, 2
	s_or_b32 s0, s0, 3
	s_cmp_lt_i32 s0, s6
	s_cselect_b64 s[2:3], -1, 0
	s_cmp_ge_i32 s0, s7
	s_cselect_b64 s[4:5], -1, 0
	s_or_b64 s[2:3], s[2:3], s[4:5]
	s_and_b64 vcc, exec, s[2:3]
	s_cbranch_vccnz .LBB0_3126
	v_readlane_b32 s2, v253, 3
	v_readlane_b32 s18, v253, 61
	s_cmp_le_i32 s0, s2
	v_readlane_b32 s19, v253, 62
	v_readlane_b32 s3, v253, 4
	s_cbranch_scc1 .LBB0_3069
	s_waitcnt vmcnt(0)
	s_waitcnt vmcnt(0) lgkmcnt(0)
	s_barrier
	s_mov_b64 s[0:1], exec
	v_readlane_b32 s2, v253, 1
	v_readlane_b32 s3, v253, 2
	s_and_b64 s[2:3], s[0:1], s[2:3]
	s_mov_b64 exec, s[2:3]
	s_cbranch_execz .LBB0_3068
	v_readlane_b32 s4, v253, 36
	v_readlane_b32 s6, v253, 11
	v_readlane_b32 s7, v253, 12
	v_readlane_b32 s8, v253, 7
	v_readlane_b32 s9, v253, 8
	s_waitcnt vmcnt(0) lgkmcnt(0)
	v_mov_b32_e32 v1, s4
	ds_read2_b32 v[2:3], v1 offset1:1
	ds_read_b32 v7, v1 offset:8
	global_atomic_add v4, v87, v230, s[8:9] sc0
	s_waitcnt lgkmcnt(0)
	v_add_u32_e32 v7, 1, v7
	ds_write_b32 v1, v7 offset:8
	v_max_u32_e32 v2, 1, v2
	v_max_u32_e32 v3, 1, v3
	v_add_u32_e32 v6, 1, v7
	v_mul_lo_u32 v5, v6, v3
	v_mul_lo_u32 v6, v6, v2
	s_waitcnt vmcnt(0)
	v_add_u32_e32 v4, 1, v4
	v_cmp_ne_u32_e32 vcc, v4, v6
	s_cbranch_vccnz .Lxb_poll_7
	buffer_wbl2 sc1
	s_waitcnt vmcnt(0)
	global_atomic_add v87, v230, s[6:7]

.LBB0_3126:
	v_readlane_b32 s0, v254, 2
	s_or_b32 s0, s0, 4
	v_readlane_b32 s6, v253, 3
	v_readlane_b32 s7, v253, 4
	s_cmp_lt_i32 s0, s6
	s_cselect_b64 s[2:3], -1, 0
	s_cmp_ge_i32 s0, s7
	s_cselect_b64 s[4:5], -1, 0
	s_or_b64 s[2:3], s[2:3], s[4:5]
	v_readlane_b32 s58, v253, 61
	s_and_b64 vcc, exec, s[2:3]
	v_readlane_b32 s59, v253, 62
	s_cbranch_vccnz .LBB0_3186
	s_cmp_le_i32 s0, s6
	s_cbranch_scc1 .LBB0_3166
	s_waitcnt vmcnt(0)
	s_waitcnt vmcnt(0) lgkmcnt(0)
	s_barrier
	s_mov_b64 s[0:1], exec
	v_readlane_b32 s2, v253, 1
	v_readlane_b32 s3, v253, 2
	s_and_b64 s[2:3], s[0:1], s[2:3]
	s_mov_b64 exec, s[2:3]
	s_cbranch_execz .LBB0_3165
	v_readlane_b32 s4, v253, 36
	v_readlane_b32 s6, v253, 11
	v_readlane_b32 s7, v253, 12
	v_readlane_b32 s8, v253, 7
	v_readlane_b32 s9, v253, 8
	s_waitcnt vmcnt(0) lgkmcnt(0)
	v_mov_b32_e32 v1, s4
	ds_read2_b32 v[2:3], v1 offset1:1
	ds_read_b32 v7, v1 offset:8
	global_atomic_add v4, v87, v230, s[8:9] sc0
	s_waitcnt lgkmcnt(0)
	v_add_u32_e32 v7, 1, v7
	ds_write_b32 v1, v7 offset:8
	v_max_u32_e32 v2, 1, v2
	v_max_u32_e32 v3, 1, v3
	v_add_u32_e32 v6, 1, v7
	v_mul_lo_u32 v5, v6, v3
	v_mul_lo_u32 v6, v6, v2
	s_waitcnt vmcnt(0)
	v_add_u32_e32 v4, 1, v4
	v_cmp_ne_u32_e32 vcc, v4, v6
	s_cbranch_vccnz .Lxb_poll_8
	buffer_wbl2 sc1
	s_waitcnt vmcnt(0)
	global_atomic_add v87, v230, s[6:7]

.LBB0_3186:
	v_readlane_b32 s0, v254, 2
	s_or_b32 s0, s0, 5
	s_cmp_lt_i32 s0, s6
	s_cselect_b64 s[2:3], -1, 0
	s_cmp_ge_i32 s0, s7
	s_cselect_b64 s[4:5], -1, 0
	s_or_b64 s[2:3], s[2:3], s[4:5]
	v_readlane_b32 s76, v253, 59
	s_and_b64 vcc, exec, s[2:3]
	v_readlane_b32 s77, v253, 60
	s_cbranch_vccnz .LBB0_3269
	v_readlane_b32 s2, v253, 3
	s_cmp_le_i32 s0, s2
	v_readlane_b32 s3, v253, 4
	s_cbranch_scc1 .LBB0_3226
	s_waitcnt vmcnt(0)
	s_waitcnt vmcnt(0) lgkmcnt(0)
	s_barrier
	s_mov_b64 s[0:1], exec
	v_readlane_b32 s2, v253, 1
	v_readlane_b32 s3, v253, 2
	s_and_b64 s[2:3], s[0:1], s[2:3]
	s_mov_b64 exec, s[2:3]
	s_cbranch_execz .LBB0_3225
	v_readlane_b32 s4, v253, 36
	v_readlane_b32 s6, v253, 11
	v_readlane_b32 s7, v253, 12
	v_readlane_b32 s8, v253, 7
	v_readlane_b32 s9, v253, 8
	s_waitcnt vmcnt(0) lgkmcnt(0)
	v_mov_b32_e32 v1, s4
	ds_read2_b32 v[2:3], v1 offset1:1
	ds_read_b32 v7, v1 offset:8
	global_atomic_add v4, v87, v230, s[8:9] sc0
	s_waitcnt lgkmcnt(0)
	v_add_u32_e32 v7, 1, v7
	ds_write_b32 v1, v7 offset:8
	v_max_u32_e32 v2, 1, v2
	v_max_u32_e32 v3, 1, v3
	v_add_u32_e32 v6, 1, v7
	v_mul_lo_u32 v5, v6, v3
	v_mul_lo_u32 v6, v6, v2
	s_waitcnt vmcnt(0)
	v_add_u32_e32 v4, 1, v4
	v_cmp_ne_u32_e32 vcc, v4, v6
	s_cbranch_vccnz .Lxb_poll_9
	buffer_wbl2 sc1
	s_waitcnt vmcnt(0)
	global_atomic_add v87, v230, s[6:7]

.LBB0_3269:
	v_readlane_b32 s0, v254, 2
	s_or_b32 s0, s0, 6
	v_readlane_b32 s12, v253, 3
	v_readlane_b32 s13, v253, 4
	s_cmp_lt_i32 s0, s12
	s_cselect_b64 s[2:3], -1, 0
	s_cmp_ge_i32 s0, s13
	s_cselect_b64 s[4:5], -1, 0
	s_or_b64 s[2:3], s[2:3], s[4:5]
	s_and_b64 vcc, exec, s[2:3]
	s_cbranch_vccnz .LBB0_3391
	s_cmp_le_i32 s0, s12
	s_cbranch_scc1 .LBB0_3309
	s_waitcnt vmcnt(0)
	s_waitcnt vmcnt(0) lgkmcnt(0)
	s_barrier
	s_mov_b64 s[0:1], exec
	v_readlane_b32 s2, v253, 1
	v_readlane_b32 s3, v253, 2
	s_and_b64 s[2:3], s[0:1], s[2:3]
	s_mov_b64 exec, s[2:3]
	s_cbranch_execz .LBB0_3308
	v_readlane_b32 s4, v253, 36
	v_readlane_b32 s6, v253, 11
	v_readlane_b32 s7, v253, 12
	v_readlane_b32 s8, v253, 7
	v_readlane_b32 s9, v253, 8
	s_waitcnt vmcnt(0) lgkmcnt(0)
	v_mov_b32_e32 v1, s4
	ds_read2_b32 v[2:3], v1 offset1:1
	ds_read_b32 v7, v1 offset:8
	global_atomic_add v4, v87, v230, s[8:9] sc0
	s_waitcnt lgkmcnt(0)
	v_add_u32_e32 v7, 1, v7
	ds_write_b32 v1, v7 offset:8
	v_max_u32_e32 v2, 1, v2
	v_max_u32_e32 v3, 1, v3
	v_add_u32_e32 v6, 1, v7
	v_mul_lo_u32 v5, v6, v3
	v_mul_lo_u32 v6, v6, v2
	s_waitcnt vmcnt(0)
	v_add_u32_e32 v4, 1, v4
	v_cmp_ne_u32_e32 vcc, v4, v6
	s_cbranch_vccnz .Lxb_poll_10
	buffer_wbl2 sc1
	s_waitcnt vmcnt(0)
	global_atomic_add v87, v230, s[6:7]

.LBB0_3391:
	v_readlane_b32 s0, v254, 2
	s_or_b32 s0, s0, 7
	s_cmp_lt_i32 s0, s12
	s_cselect_b64 s[2:3], -1, 0
	s_cmp_ge_i32 s0, s13
	s_cselect_b64 s[4:5], -1, 0
	s_or_b64 s[2:3], s[2:3], s[4:5]
	s_and_b64 vcc, exec, s[2:3]
	s_cbranch_vccnz .LBB0_3493
	s_cmp_le_i32 s0, s12
	s_cbranch_scc1 .LBB0_3431
	s_waitcnt vmcnt(0)
	s_waitcnt vmcnt(0) lgkmcnt(0)
	s_barrier
	s_mov_b64 s[0:1], exec
	v_readlane_b32 s2, v253, 1
	v_readlane_b32 s3, v253, 2
	s_and_b64 s[2:3], s[0:1], s[2:3]
	s_mov_b64 exec, s[2:3]
	s_cbranch_execz .LBB0_3430
	v_readlane_b32 s4, v253, 36
	v_readlane_b32 s6, v253, 11
	v_readlane_b32 s7, v253, 12
	v_readlane_b32 s8, v253, 7
	v_readlane_b32 s9, v253, 8
	s_waitcnt vmcnt(0) lgkmcnt(0)
	v_mov_b32_e32 v1, s4
	ds_read2_b32 v[2:3], v1 offset1:1
	ds_read_b32 v7, v1 offset:8
	global_atomic_add v4, v87, v230, s[8:9] sc0
	s_waitcnt lgkmcnt(0)
	v_add_u32_e32 v7, 1, v7
	ds_write_b32 v1, v7 offset:8
	v_max_u32_e32 v2, 1, v2
	v_max_u32_e32 v3, 1, v3
	v_add_u32_e32 v6, 1, v7
	v_mul_lo_u32 v5, v6, v3
	v_mul_lo_u32 v6, v6, v2
	s_waitcnt vmcnt(0)
	v_add_u32_e32 v4, 1, v4
	v_cmp_ne_u32_e32 vcc, v4, v6
	s_cbranch_vccnz .Lxb_poll_11
	buffer_wbl2 sc1
	s_waitcnt vmcnt(0)
	global_atomic_add v87, v230, s[6:7]

.LBB0_3494:
	v_readlane_b32 s2, v253, 3
	s_cmp_le_i32 s0, s2
	v_readlane_b32 s3, v253, 4
	s_cbranch_scc1 .LBB0_3533
	s_waitcnt vmcnt(0)
	s_waitcnt vmcnt(0) lgkmcnt(0)
	s_barrier
	s_mov_b64 s[0:1], exec
	v_readlane_b32 s2, v253, 1
	v_readlane_b32 s3, v253, 2
	s_and_b64 s[2:3], s[0:1], s[2:3]
	s_mov_b64 exec, s[2:3]
	s_cbranch_execz .LBB0_3532
	v_readlane_b32 s4, v253, 36
	v_readlane_b32 s6, v253, 11
	v_readlane_b32 s7, v253, 12
	v_readlane_b32 s8, v253, 7
	v_readlane_b32 s9, v253, 8
	s_waitcnt vmcnt(0) lgkmcnt(0)
	v_mov_b32_e32 v1, s4
	ds_read2_b32 v[2:3], v1 offset1:1
	ds_read_b32 v7, v1 offset:8
	global_atomic_add v4, v87, v230, s[8:9] sc0
	s_waitcnt lgkmcnt(0)
	v_add_u32_e32 v7, 1, v7
	ds_write_b32 v1, v7 offset:8
	v_max_u32_e32 v2, 1, v2
	v_max_u32_e32 v3, 1, v3
	v_add_u32_e32 v6, 1, v7
	v_mul_lo_u32 v5, v6, v3
	v_mul_lo_u32 v6, v6, v2
	s_waitcnt vmcnt(0)
	v_add_u32_e32 v4, 1, v4
	v_cmp_ne_u32_e32 vcc, v4, v6
	s_cbranch_vccnz .Lxb_poll_12
	buffer_wbl2 sc1
	s_waitcnt vmcnt(0)
	global_atomic_add v87, v230, s[6:7]
